# adds P7 router-logit loop: next iteration's h rows + w_router dwords loaded one iteration ahead
# speedup vs baseline: 1.0079x; 1.0079x over previous
; #define LAS __attribute__((address_space(3)))
; __device__ __forceinline__ void p7_router(Frame& F, const Args& A, bool commit = true) {
;     ...
;         for (int k = F.tid; k < DM; k += 512) { gainL[k] = A.in[I_N2G][k] * (1.0f + mod[4 * DM + k]); shiftL[k] = mod[3 * DM + k]; }
;         if (F.tid < 32) lcnt[F.tid] = 0;
;         __syncthreads();
;         {
;             const int i = F.lane & 31, kk = F.lane >> 5, kb = F.wave * 256 + kk * 128;
;             const float* hp = H1 + (size_t)(t0 + i) * DM + kb; const float* wp = A.in[I_WR] + (size_t)kb * 32 + i; const LAS float* gp = gainL + kb;
;             f32x16r acc = {}; float ss = 0.f;
; #pragma unroll 4
;             for (int s0 = 0; s0 < 128; s0 += 4) {
;                 const f32x4 hv = *(const f32x4*)(hp + s0); const f32x4 g4 = *(const LAS f32x4*)(gp + s0);
;                 const float b0 = wp[(s0 + 0) * 32], b1 = wp[(s0 + 1) * 32], b2 = wp[(s0 + 2) * 32], b3 = wp[(s0 + 3) * 32];
.LBB0_891:
	global_load_dword v10, v[4:5], off
	global_load_dword v11, v[2:3], off
	v_add_co_u32_e32 v8, vcc, 0xffffe000, v2
	v_add_u32_e32 v7, 0x200, v7
	s_nop 0
	v_addc_co_u32_e32 v9, vcc, -1, v3, vcc
	global_load_dword v8, v[8:9], off
	v_cmp_lt_u32_e32 vcc, s33, v7
	v_lshl_add_u64 v[4:5], v[4:5], 0, s[38:39]
	v_lshl_add_u64 v[2:3], v[2:3], 0, s[38:39]
	s_or_b64 s[6:7], vcc, s[6:7]
	s_waitcnt vmcnt(0)
	v_add_f32_e32 v9, 1.0, v11
	v_mul_f32_e32 v9, v10, v9
	ds_write2st64_b32 v6, v9, v8 offset1:32
	v_add_u32_e32 v6, 0x800, v6
	s_andn2_b64 exec, exec, s[6:7]
	s_cbranch_execnz .LBB0_891
	s_or_b64 exec, exec, s[6:7]
	s_and_saveexec_b64 s[6:7], s[4:5]
	ds_write_b32 v203, v71 offset:55552
	s_or_b64 exec, exec, s[6:7]
	v_ashrrev_i32_e32 v89, 31, v88
	v_lshlrev_b64 v[2:3], 13, v[88:89]
	v_mov_b32_e32 v22, 0
	v_lshl_add_u64 v[18:19], v[86:87], 0, v[2:3]
	s_mov_b32 s6, -4
	v_mov_b64_e32 v[20:21], v[90:91]
	v_mov_b32_e32 v23, v101
	v_mov_b32_e32 v2, 0
	v_mov_b32_e32 v3, v22
	v_mov_b32_e32 v4, v22
	v_mov_b32_e32 v5, v22
	v_mov_b32_e32 v6, v22
	v_mov_b32_e32 v7, v22
	v_mov_b32_e32 v8, v22
	v_mov_b32_e32 v9, v22
	v_mov_b32_e32 v10, v22
	v_mov_b32_e32 v11, v22
	v_mov_b32_e32 v12, v22
	v_mov_b32_e32 v13, v22
	v_mov_b32_e32 v14, v22
	v_mov_b32_e32 v15, v22
	v_mov_b32_e32 v16, v22
	v_mov_b32_e32 v17, v22
	s_waitcnt lgkmcnt(0)
	s_barrier
	global_load_dwordx4 v[230:233], v[18:19], off offset:-48
	global_load_dwordx4 v[234:237], v[18:19], off offset:-32
	global_load_dwordx4 v[238:241], v[18:19], off offset:-16
	global_load_dwordx4 v[242:245], v[18:19], off
	global_load_dword v248, v[20:21], off offset:-1920
	global_load_dword v249, v[20:21], off offset:-1792
	global_load_dword v250, v[20:21], off offset:-1664
	global_load_dword v251, v[20:21], off offset:-1536
	global_load_dword v252, v[20:21], off offset:-1408
	global_load_dword v253, v[20:21], off offset:-1280
	global_load_dword v254, v[20:21], off offset:-1152
	global_load_dword v255, v[20:21], off offset:-1024
	global_load_dword v200, v[20:21], off offset:-896
	global_load_dword v201, v[20:21], off offset:-768
	global_load_dword v202, v[20:21], off offset:-640
	global_load_dword v204, v[20:21], off offset:-512
	global_load_dword v205, v[20:21], off offset:-384
	global_load_dword v109, v[20:21], off offset:-256
	global_load_dword v119, v[20:21], off offset:-128
	global_load_dword v189, v[20:21], off
; #define LAS __attribute__((address_space(3)))
; __device__ __forceinline__ void p7_router(Frame& F, const Args& A, bool commit = true) {
;     ...
; #pragma unroll 4
;             for (int s0 = 0; s0 < 128; s0 += 4) {
;                 const f32x4 hv = *(const f32x4*)(hp + s0); const f32x4 g4 = *(const LAS f32x4*)(gp + s0);
;                 const float b0 = wp[(s0 + 0) * 32], b1 = wp[(s0 + 1) * 32], b2 = wp[(s0 + 2) * 32], b3 = wp[(s0 + 3) * 32];
;                 ss += (hv.x * hv.x + hv.y * hv.y) + (hv.z * hv.z + hv.w * hv.w);
;                 acc = __builtin_amdgcn_mfma_f32_32x32x2f32(hv.x * g4.x, b0, acc, 0, 0, 0);
;                 acc = __builtin_amdgcn_mfma_f32_32x32x2f32(hv.y * g4.y, b1, acc, 0, 0, 0);
;                 acc = __builtin_amdgcn_mfma_f32_32x32x2f32(hv.z * g4.z, b2, acc, 0, 0, 0);
;                 acc = __builtin_amdgcn_mfma_f32_32x32x2f32(hv.w * g4.w, b3, acc, 0, 0, 0);
;             }
; #pragma unroll
;             for (int r = 0; r < 16; ++r) part[(F.wave * 32 + (r & 3) + 8 * (r >> 2) + 4 * kk) * 32 + i] = acc[r];
;             ssp[F.wave * 64 + F.lane] = ss;
.LBB0_895:
	s_add_i32 s6, s6, 16
	s_cmpk_gt_u32 s6, 0x7b
	ds_read_b128 v[110:113], v23
	ds_read_b128 v[114:117], v23 offset:16
	s_cselect_b64 s[98:99], 0, s[38:39]
	s_cselect_b64 s[100:101], 0, 64
	s_waitcnt vmcnt(0)
	v_mov_b64_e32 v[24:25], v[230:231]
	v_mov_b64_e32 v[26:27], v[232:233]
	v_mov_b64_e32 v[28:29], v[234:235]
	v_mov_b64_e32 v[30:31], v[236:237]
	v_mov_b64_e32 v[36:37], v[238:239]
	v_mov_b64_e32 v[38:39], v[240:241]
	v_mov_b64_e32 v[32:33], v[242:243]
	v_mov_b64_e32 v[34:35], v[244:245]
	v_mov_b32_e32 v40, v248
	v_mov_b32_e32 v41, v249
	v_mov_b32_e32 v42, v250
	v_mov_b32_e32 v43, v251
	v_mov_b32_e32 v44, v252
	v_mov_b32_e32 v45, v253
	v_mov_b32_e32 v46, v254
	v_mov_b32_e32 v47, v255
	v_mov_b32_e32 v48, v200
	v_mov_b32_e32 v49, v201
	v_mov_b32_e32 v50, v202
	v_mov_b32_e32 v51, v204
	v_mov_b32_e32 v196, v205
	v_mov_b32_e32 v197, v109
	v_mov_b32_e32 v198, v119
	v_mov_b32_e32 v199, v189
	v_lshl_add_u64 v[18:19], v[18:19], 0, s[100:101]
	v_lshl_add_u64 v[20:21], v[20:21], 0, s[98:99]
	global_load_dwordx4 v[230:233], v[18:19], off offset:-48
	global_load_dwordx4 v[234:237], v[18:19], off offset:-32
	global_load_dwordx4 v[238:241], v[18:19], off offset:-16
	global_load_dwordx4 v[242:245], v[18:19], off
	global_load_dword v248, v[20:21], off offset:-1920
	global_load_dword v249, v[20:21], off offset:-1792
	global_load_dword v250, v[20:21], off offset:-1664
	global_load_dword v251, v[20:21], off offset:-1536
	global_load_dword v252, v[20:21], off offset:-1408
	global_load_dword v253, v[20:21], off offset:-1280
	global_load_dword v254, v[20:21], off offset:-1152
	global_load_dword v255, v[20:21], off offset:-1024
	global_load_dword v200, v[20:21], off offset:-896
	global_load_dword v201, v[20:21], off offset:-768
	global_load_dword v202, v[20:21], off offset:-640
	global_load_dword v204, v[20:21], off offset:-512
	global_load_dword v205, v[20:21], off offset:-384
	global_load_dword v109, v[20:21], off offset:-256
	global_load_dword v119, v[20:21], off offset:-128
	global_load_dword v189, v[20:21], off
	s_waitcnt lgkmcnt(1)
	v_mul_f32_e32 v192, v24, v110
	s_nop 1
	v_mfma_f32_32x32x2_f32 v[2:17], v192, v40, v[2:17]
	v_mul_f32_e32 v192, v25, v111
	v_mul_f32_e64 v24, v24, v24
	v_mul_f32_e64 v25, v25, v25
	v_mfma_f32_32x32x2_f32 v[2:17], v192, v41, v[2:17]
	v_mul_f32_e32 v192, v26, v112
	s_nop 1
	v_mfma_f32_32x32x2_f32 v[2:17], v192, v42, v[2:17]
	v_mul_f32_e32 v192, v27, v113
	v_mul_f32_e64 v26, v26, v26
	v_mul_f32_e64 v27, v27, v27
	v_mfma_f32_32x32x2_f32 v[2:17], v192, v43, v[2:17]
	s_waitcnt lgkmcnt(0)
	v_mul_f32_e32 v192, v28, v114
	s_nop 1
	v_mfma_f32_32x32x2_f32 v[2:17], v192, v44, v[2:17]
	v_mul_f32_e32 v192, v29, v115
	v_mul_f32_e64 v28, v28, v28
	v_mul_f32_e64 v29, v29, v29
	v_mfma_f32_32x32x2_f32 v[2:17], v192, v45, v[2:17]
	v_mul_f32_e32 v192, v30, v116
	s_nop 1
	v_mfma_f32_32x32x2_f32 v[2:17], v192, v46, v[2:17]
	v_mul_f32_e32 v192, v31, v117
	v_mul_f32_e64 v30, v30, v30
	v_mul_f32_e64 v31, v31, v31
	v_mfma_f32_32x32x2_f32 v[2:17], v192, v47, v[2:17]
	ds_read_b128 v[110:113], v23 offset:32
	ds_read_b128 v[114:117], v23 offset:48
	v_add_u32_e32 v23, 64, v23
	s_waitcnt lgkmcnt(1)
	v_mul_f32_e32 v192, v36, v110
	s_nop 1
	v_mfma_f32_32x32x2_f32 v[2:17], v192, v48, v[2:17]
	v_mul_f32_e32 v192, v37, v111
	v_mul_f32_e64 v36, v36, v36
	v_mul_f32_e64 v37, v37, v37
	v_mfma_f32_32x32x2_f32 v[2:17], v192, v49, v[2:17]
	v_mul_f32_e32 v192, v38, v112
	s_nop 1
	v_mfma_f32_32x32x2_f32 v[2:17], v192, v50, v[2:17]
	v_mul_f32_e32 v192, v39, v113
	v_mul_f32_e64 v38, v38, v38
	v_mul_f32_e64 v39, v39, v39
	v_mfma_f32_32x32x2_f32 v[2:17], v192, v51, v[2:17]
	s_waitcnt lgkmcnt(0)
	v_mul_f32_e32 v192, v32, v114
	s_nop 1
	v_mfma_f32_32x32x2_f32 v[2:17], v192, v196, v[2:17]
	v_mul_f32_e32 v192, v33, v115
	v_mul_f32_e64 v32, v32, v32
	v_mul_f32_e64 v33, v33, v33
	v_mfma_f32_32x32x2_f32 v[2:17], v192, v197, v[2:17]
	v_mul_f32_e32 v192, v34, v116
	v_mul_f32_e32 v193, v35, v117
	s_nop 0
	v_mfma_f32_32x32x2_f32 v[2:17], v192, v198, v[2:17]
	v_mul_f32_e64 v40, v34, v34
	v_mul_f32_e64 v41, v35, v35
	v_pk_mov_b32 v[34:35], v[24:25], v[26:27] op_sel:[1,0]
	v_mov_b32_e32 v25, v27
	v_pk_mov_b32 v[26:27], v[28:29], v[30:31] op_sel:[1,0]
	v_mov_b32_e32 v29, v31
	v_pk_add_f32 v[24:25], v[34:35], v[24:25]
	v_pk_mov_b32 v[30:31], v[36:37], v[38:39] op_sel:[1,0]
	v_mov_b32_e32 v37, v39
	v_pk_add_f32 v[26:27], v[26:27], v[28:29]
	v_add_f32_e32 v24, v24, v25
	v_pk_mov_b32 v[38:39], v[32:33], v[40:41] op_sel:[1,0]
	v_mov_b32_e32 v33, v41
	v_pk_add_f32 v[28:29], v[30:31], v[36:37]
	v_add_f32_e32 v25, v26, v27
	v_add_f32_e32 v22, v22, v24
	v_mfma_f32_32x32x2_f32 v[2:17], v193, v199, v[2:17]
	v_add_f32_e64 v30, v38, v32
	v_add_f32_e64 v31, v39, v33
	v_add_f32_e32 v26, v28, v29
	v_add_f32_e32 v22, v22, v25
	v_add_f32_e32 v27, v30, v31
	v_add_f32_e32 v22, v22, v26
	v_add_f32_e32 v22, v22, v27
	s_cbranch_scc0 .LBB0_895
	v_add_u32_e32 v18, 0x4000, v102
	s_nop 8
	ds_write2_b32 v18, v2, v3 offset1:32
	ds_write2_b32 v18, v4, v5 offset0:64 offset1:96
	v_add_u32_e32 v2, 0x4400, v102
	ds_write2_b32 v2, v6, v7 offset1:32
	ds_write2_b32 v2, v8, v9 offset0:64 offset1:96
	v_add_u32_e32 v2, 0x4800, v102
	ds_write2_b32 v2, v10, v11 offset1:32
	ds_write2_b32 v2, v12, v13 offset0:64 offset1:96
	v_add_u32_e32 v2, 0x4c00, v102
	ds_write2_b32 v2, v14, v15 offset1:32
	ds_write2_b32 v2, v16, v17 offset0:64 offset1:96
	ds_write_b32 v103, v22 offset:49152
	s_waitcnt lgkmcnt(0)
	s_barrier
	global_load_dword v26, v[72:73], off
	v_add_u32_e32 v2, 0xc000, v92
	ds_read2_b32 v[24:25], v2 offset1:32
	ds_read2_b32 v[22:23], v2 offset0:64 offset1:96
	ds_read2_b32 v[20:21], v2 offset0:128 offset1:160
	ds_read2_b32 v[16:17], v2 offset0:192 offset1:224
	v_add_u32_e32 v2, 0xc400, v92
	ds_read2_b32 v[18:19], v2 offset1:32
	ds_read2_b32 v[14:15], v2 offset0:64 offset1:96
	ds_read2_b32 v[12:13], v2 offset0:128 offset1:160
	ds_read2_b32 v[10:11], v2 offset0:192 offset1:224
	ds_read2st64_b32 v[8:9], v94 offset0:64 offset1:80
	ds_read2st64_b32 v[6:7], v94 offset0:96 offset1:112
	ds_read2st64_b32 v[4:5], v94 offset0:128 offset1:144
	ds_read2st64_b32 v[2:3], v94 offset0:160 offset1:176
	s_lshl_b32 s44, s44, 10
	v_or_b32_e32 v27, s44, v93
	s_mov_b32 s6, 0
